# k_iter first: prologue target+SBB8 loads issued together; candidate gather of round r+1 prefetched during round r
# speedup vs baseline: 1.0293x; 1.0055x over previous
_Z6k_iterILb1ELb0EEvPKfS1_PKiPK15HIP_vector_typeIfLj4EES7_S1_S1_S3_S1_PfS8_S1_S3_PDF16_PS5_SA_PiSA_SB_:
	s_load_dwordx2 s[4:5], s[0:1], 0x78
	s_load_dwordx8 s[20:27], s[0:1], 0x20
	s_load_dwordx2 s[92:93], s[0:1], 0x18
	v_readfirstlane_b32 s54, v0
	v_cmp_gt_u32_e64 s[8:9], 64, v0
	v_lshlrev_b32_e32 v46, 2, v0
	s_and_saveexec_b64 s[6:7], s[8:9]
	v_mov_b32_e32 v1, 0
	ds_write_b32 v46, v1 offset:29728
	s_or_b64 exec, exec, s[6:7]
	s_lshl_b32 s3, s2, 5
	s_and_b32 s3, s3, 0xe0
	s_lshr_b32 s2, s2, 3
	s_add_i32 s46, s3, s2
	s_lshr_b32 s12, s46, 6
	s_lshl_b32 s13, s46, 6
	s_mov_b32 s47, 0
	s_and_b32 s33, s13, 0xfc0
	s_lshl_b32 s58, s12, 12
	s_lshl_b64 s[2:3], s[46:47], 4
	s_waitcnt lgkmcnt(0)
	s_add_u32 s6, s20, s2
	v_and_b32_e32 v25, 31, v0
	s_addc_u32 s7, s21, s3
	s_or_b32 s59, s58, s33
	v_or_b32_e32 v6, s59, v25
	v_mov_b32_e32 v7, 0
	v_lshlrev_b64 v[2:3], 2, v[6:7]
	v_lshl_add_u64 v[4:5], s[22:23], 0, v[2:3]
	v_lshl_add_u64 v[8:9], s[24:25], 0, v[2:3]
	v_lshl_add_u64 v[2:3], s[26:27], 0, v[2:3]
	global_load_dword v196, v[4:5], off offset:128
	global_load_dword v197, v[8:9], off offset:128
	global_load_dword v198, v[2:3], off offset:128
	global_load_dword v4, v[4:5], off
	global_load_dword v5, v[8:9], off
	global_load_dword v6, v[2:3], off
	s_lshl_b32 s94, s12, 13
	s_add_u32 s94, s92, s94
	s_addc_u32 s95, s93, 0
	v_lshlrev_b32_e32 v199, 4, v0
	global_load_dwordx4 v[192:195], v199, s[94:95]
	s_load_dwordx4 s[36:39], s[6:7], 0x0
	s_bfe_u32 s14, s54, 0x10006
	s_cmpk_lt_u32 s54, 0x80
	s_cselect_b64 s[6:7], -1, 0
	s_waitcnt lgkmcnt(0)
	v_mov_b64_e32 v[2:3], s[38:39]
	v_pk_add_f32 v[2:3], s[36:37], v[2:3]
	s_cmp_eq_u32 s14, 0
	v_pk_mul_f32 v[22:23], v[2:3], 0.5 op_sel_hi:[1,0]
	v_and_b32_e32 v44, 63, v0
	s_cselect_b64 s[10:11], -1, 0
	v_mov_b32_e32 v1, 0xff800000
	v_cmp_gt_u32_e64 s[18:19], 32, v44
	s_and_b64 s[10:11], s[10:11], s[6:7]
	s_and_b64 s[16:17], s[10:11], s[18:19]
	v_lshlrev_b32_e32 v10, 4, v25
	s_waitcnt vmcnt(2)
	v_pk_fma_f32 v[36:37], v[2:3], 0.5, v[4:5] op_sel_hi:[1,0,1] neg_lo:[1,0,0] neg_hi:[1,0,0]
	s_nop 0
	v_pk_mul_f32 v[2:3], v[36:37], v[36:37]
	s_waitcnt vmcnt(1)
	v_cmp_ne_u32_e32 vcc, 0, v6
	v_add_f32_e32 v2, v2, v3
	v_sub_f32_e32 v2, 0x3d23d70a, v2
	v_mul_f32_e32 v2, 0x431044f5, v2
	v_cndmask_b32_e32 v4, v1, v2, vcc
	s_and_saveexec_b64 s[10:11], s[16:17]
	s_cbranch_execz .LBB2_4
	s_mov_b32 s16, 0x439044f5
	v_or_b32_e32 v6, s13, v25
	v_pk_mul_f32 v[2:3], v[36:37], s[16:17] op_sel_hi:[1,0]
	v_mov_b32_e32 v5, v7
	v_lshl_add_u64 v[8:9], v[6:7], 4, s[4:5]
	ds_write_b128 v10, v[2:5] offset:26656
	global_store_dwordx4 v[8:9], v[2:5], off
.LBB2_4:
	s_or_b64 exec, exec, s[10:11]
	s_cmp_lg_u32 s14, 0
	s_cselect_b64 s[10:11], -1, 0
	s_and_b64 s[6:7], s[10:11], s[6:7]
	s_and_b64 s[10:11], s[6:7], s[18:19]
	v_pk_add_f32 v[2:3], v[196:197], v[22:23] neg_lo:[0,1] neg_hi:[0,1]
	s_nop 0
	v_pk_mul_f32 v[6:7], v[2:3], v[2:3]
	v_cmp_ne_u32_e32 vcc, 0, v198
	v_add_f32_e32 v6, v6, v7
	v_sub_f32_e32 v6, 0x3d23d70a, v6
	v_mul_f32_e32 v6, 0x431044f5, v6
	v_cndmask_b32_e32 v8, v1, v6, vcc
	s_and_saveexec_b64 s[6:7], s[10:11]
	s_cbranch_execz .LBB2_6
	s_mov_b32 s10, 0x439044f5
	v_pk_mul_f32 v[6:7], v[2:3], s[10:11] op_sel_hi:[1,0]
	v_mov_b32_e32 v9, 0
	ds_write_b128 v10, v[6:9] offset:27168
	v_add_u32_e32 v10, s13, v25
	v_mov_b32_e32 v11, v9
	v_lshl_add_u64 v[10:11], v[10:11], 4, s[4:5]
	global_store_dwordx4 v[10:11], v[6:9], off offset:512
.LBB2_6:
	s_or_b64 exec, exec, s[6:7]
	s_lshl_b32 s26, s12, 9
	s_mov_b32 s27, 0
	v_lshlrev_b32_e32 v6, 4, v0
	s_load_dwordx2 s[6:7], s[0:1], 0x70
	s_mov_b32 s2, 0x3d23dc48
	v_mov_b32_e32 v1, 0
	v_cmp_eq_u32_e32 vcc, 0, v44
	s_waitcnt vmcnt(0)
	v_subrev_f32_e32 v5, s38, v192
	v_sub_f32_e32 v7, s36, v194
	v_subrev_f32_e32 v9, s39, v193
	v_sub_f32_e32 v11, s37, v195
	v_max3_f32 v10, v5, v7, 0
	v_max3_f32 v11, v9, v11, 0
	v_pk_mul_f32 v[10:11], v[10:11], v[10:11]
	s_nop 0
	v_add_f32_e32 v5, v10, v11
	v_cmp_gt_f32_e64 s[2:3], s2, v5
	s_and_saveexec_b64 s[4:5], vcc
	s_xor_b64 s[4:5], exec, s[4:5]
	s_bcnt1_i32_b64 s10, s[2:3]
	v_lshrrev_b32_e32 v5, 4, v0
	v_mov_b32_e32 v7, s10
	ds_write_b32 v5, v7 offset:26624
	s_or_b64 exec, exec, s[4:5]
	s_waitcnt lgkmcnt(0)
	s_barrier
	ds_read_b128 v[14:17], v1 offset:26624
	ds_read_b128 v[10:13], v1 offset:26640
	v_lshlrev_b64 v[18:19], v44, -1
	s_and_saveexec_b64 s[10:11], s[2:3]
	s_cbranch_execz .LBB2_10
	s_movk_i32 s4, 0x1ff
	v_cmp_lt_u32_e64 s[4:5], s4, v0
	v_bfi_b32 v28, v18, 0, s2
	v_bfi_b32 v27, v19, 0, s3
	s_waitcnt lgkmcnt(0)
	v_cndmask_b32_e64 v1, 0, v13, s[4:5]
	s_movk_i32 s4, 0x1bf
	v_cmp_lt_u32_e64 s[4:5], s4, v0
	v_lshlrev_b32_e32 v1, 2, v1
	v_bcnt_u32_b32 v28, v28, 0
	v_cndmask_b32_e64 v5, 0, v12, s[4:5]
	s_movk_i32 s4, 0x17f
	v_cmp_lt_u32_e64 s[4:5], s4, v0
	v_lshlrev_b32_e32 v5, 2, v5
	v_cndmask_b32_e64 v26, v14, 0, s[8:9]
	v_cndmask_b32_e64 v7, 0, v11, s[4:5]
	s_movk_i32 s4, 0x13f
	v_cmp_lt_u32_e64 s[4:5], s4, v0
	v_lshlrev_b32_e32 v7, 2, v7
	v_add3_u32 v1, v1, v5, v7
	v_cndmask_b32_e64 v9, 0, v10, s[4:5]
	s_movk_i32 s4, 0xff
	v_cmp_lt_u32_e64 s[4:5], s4, v0
	v_lshlrev_b32_e32 v5, 2, v9
	v_bcnt_u32_b32 v27, v27, v28
	v_cndmask_b32_e64 v20, 0, v17, s[4:5]
	s_movk_i32 s4, 0xbf
	v_cmp_lt_u32_e64 s[4:5], s4, v0
	v_lshlrev_b32_e32 v7, 2, v20
	v_add3_u32 v1, v1, v5, v7
	v_cndmask_b32_e64 v21, 0, v16, s[4:5]
	s_movk_i32 s4, 0x7f
	v_cmp_lt_u32_e64 s[4:5], s4, v0
	v_lshlrev_b32_e32 v5, 2, v21
	s_nop 0
	v_cndmask_b32_e64 v24, 0, v15, s[4:5]
	v_lshlrev_b32_e32 v7, 2, v24
	v_add3_u32 v1, v1, v5, v7
	v_lshlrev_b32_e32 v5, 2, v26
	v_lshlrev_b32_e32 v7, 2, v27
	v_add3_u32 v1, v1, v5, v7
	ds_write_b32 v1, v0 offset:24576
.LBB2_10:
	s_or_b64 exec, exec, s[10:11]
	s_waitcnt lgkmcnt(1)
	v_add_u32_e32 v1, v15, v14
	v_add_u32_e32 v1, v1, v16
	v_add_u32_e32 v1, v1, v17
	s_waitcnt lgkmcnt(0)
	v_add_u32_e32 v1, v1, v10
	v_add_u32_e32 v1, v1, v11
	s_load_dwordx2 s[48:49], s[0:1], 0x90
	s_load_dwordx2 s[50:51], s[0:1], 0x80
	s_load_dwordx4 s[28:31], s[0:1], 0x60
	s_load_dwordx2 s[34:35], s[0:1], 0x48
	v_add_u32_e32 v1, v1, v12
	v_add_u32_e32 v1, v1, v13
	s_lshr_b32 s27, s54, 6
	v_readfirstlane_b32 s2, v1
	s_lshl_b32 s60, s2, 3
	s_lshl_b64 s[20:21], s[46:47], 16
	s_add_u32 s44, s6, s20
	s_addc_u32 s45, s7, s21
	s_cmp_lt_i32 s2, 1
	s_waitcnt lgkmcnt(0)
	s_barrier
	s_cbranch_scc1 .LBB2_20
	s_lshl_b32 s47, s27, 2
	s_addk_i32 s47, 0x6000
	s_cmpk_gt_u32 s54, 0x1ff
	s_cselect_b64 s[2:3], -1, 0
	s_cmpk_gt_u32 s54, 0x1bf
	s_cselect_b64 s[4:5], -1, 0
	s_cmpk_gt_u32 s54, 0x17f
	s_cselect_b64 s[6:7], -1, 0
	s_cmpk_gt_u32 s54, 0x13f
	s_cselect_b64 s[10:11], -1, 0
	s_cmpk_gt_u32 s54, 0xff
	s_load_dwordx2 s[22:23], s[0:1], 0x88
	s_load_dwordx4 s[40:43], s[0:1], 0x0
	s_load_dwordx2 s[52:53], s[0:1], 0x10
	s_cselect_b64 s[12:13], -1, 0
	s_cmpk_gt_u32 s54, 0xbf
	s_cselect_b64 s[14:15], -1, 0
	s_cmpk_gt_u32 s54, 0x7f
	s_cselect_b64 s[16:17], -1, 0
	s_cmp_lt_u32 s54, 64
	s_cselect_b64 s[54:55], -1, 0
	s_waitcnt lgkmcnt(0)
	s_add_u32 s20, s22, s20
	v_mov_b32_e32 v7, 0
	s_addc_u32 s21, s23, s21
	v_lshl_add_u64 v[10:11], s[20:21], 0, v[6:7]
	v_and_b32_e32 v5, 7, v0
	v_not_b32_e32 v1, v19
	v_not_b32_e32 v24, v18
	v_lshl_add_u64 v[26:27], v[10:11], 0, 8
	v_lshrrev_b32_e32 v9, 3, v0
	s_mov_b32 s61, 0
	s_mov_b32 s62, 0x3d23dc48
	s_movk_i32 s63, 0x600
	s_mov_b64 s[56:57], 0x2000
	v_mov_b32_e32 v30, 0xff800000
	v_mov_b32_e32 v6, 0
	v_cmp_gt_i32_e64 s[20:21], s60, v0
	s_nop 1
	v_cndmask_b32_e64 v10, 0, v9, s[20:21]
	v_lshlrev_b32_e32 v10, 2, v10
	ds_read_b32 v10, v10 offset:24576
	s_waitcnt lgkmcnt(0)
	v_lshl_or_b32 v187, v10, 3, v5
	v_add_u32_e32 v10, s58, v187
	v_ashrrev_i32_e32 v11, 31, v10
	v_lshlrev_b64 v[10:11], 2, v[10:11]
	v_lshl_add_u64 v[16:17], s[40:41], 0, v[10:11]
	v_lshl_add_u64 v[18:19], s[42:43], 0, v[10:11]
	v_lshl_add_u64 v[10:11], s[52:53], 0, v[10:11]
	global_load_dword v184, v[16:17], off
	global_load_dword v185, v[18:19], off
	global_load_dword v186, v[10:11], off
	s_branch .LBB2_13

.LBB2_13:
	v_add_u32_e32 v10, s61, v0
	v_cmp_gt_i32_e64 s[20:21], s60, v10
	v_add_u32_e32 v10, 0x200, v10
	v_cmp_gt_i32_e64 s[22:23], s60, v10
	v_add_u32_e32 v11, 64, v9
	s_nop 1
	v_cndmask_b32_e64 v10, 0, v11, s[22:23]
	v_lshlrev_b32_e32 v10, 2, v10
	ds_read_b32 v10, v10 offset:24576
	s_waitcnt vmcnt(0)
	v_mov_b32_e32 v14, v184
	v_mov_b32_e32 v15, v185
	v_mov_b32_e32 v12, v186
	v_mov_b32_e32 v13, v187
	s_waitcnt lgkmcnt(0)
	v_lshl_or_b32 v187, v10, 3, v5
	v_add_u32_e32 v10, s58, v187
	v_ashrrev_i32_e32 v11, 31, v10
	v_lshlrev_b64 v[10:11], 2, v[10:11]
	v_lshl_add_u64 v[16:17], s[40:41], 0, v[10:11]
	v_lshl_add_u64 v[18:19], s[42:43], 0, v[10:11]
	v_lshl_add_u64 v[10:11], s[52:53], 0, v[10:11]
	global_load_dword v184, v[16:17], off
	global_load_dword v185, v[18:19], off
	global_load_dword v186, v[10:11], off
	v_pk_add_f32 v[10:11], v[14:15], v[22:23] neg_lo:[0,1] neg_hi:[0,1]
	s_nop 0
	v_pk_mul_f32 v[16:17], v[10:11], v[10:11]
	v_cmp_ne_u32_e64 s[22:23], 0, v12
	v_add_f32_e32 v12, v16, v17
	v_mul_f32_e32 v12, 0xc31044f5, v12
	s_and_saveexec_b64 s[24:25], s[20:21]
	s_cbranch_execz .LBB2_15
	v_cndmask_b32_e64 v18, v30, v12, s[22:23]
	v_mov_b32_e32 v16, v10
	v_mov_b32_e32 v17, v11
	v_mov_b32_e32 v19, v13
	global_store_dwordx4 v[26:27], v[16:19], off offset:-8

	.amdhsa_kernel _Z6k_iterILb1ELb0EEvPKfS1_PKiPK15HIP_vector_typeIfLj4EES7_S1_S1_S3_S1_PfS8_S1_S3_PDF16_PS5_SA_PiSA_SB_
		.amdhsa_group_segment_fixed_size 30384
		.amdhsa_private_segment_fixed_size 0
		.amdhsa_kernarg_size 152
		.amdhsa_user_sgpr_count 2
		.amdhsa_user_sgpr_dispatch_ptr 0
		.amdhsa_user_sgpr_queue_ptr 0
		.amdhsa_user_sgpr_kernarg_segment_ptr 1
		.amdhsa_user_sgpr_dispatch_id 0
		.amdhsa_user_sgpr_kernarg_preload_length 0
		.amdhsa_user_sgpr_kernarg_preload_offset 0
		.amdhsa_user_sgpr_private_segment_size 0
		.amdhsa_uses_dynamic_stack 0
		.amdhsa_enable_private_segment 0
		.amdhsa_system_sgpr_workgroup_id_x 1
		.amdhsa_system_sgpr_workgroup_id_y 0
		.amdhsa_system_sgpr_workgroup_id_z 0
		.amdhsa_system_sgpr_workgroup_info 0
		.amdhsa_system_vgpr_workitem_id 0
		.amdhsa_next_free_vgpr 216
		.amdhsa_next_free_sgpr 96
		.amdhsa_accum_offset 216
		.amdhsa_reserve_vcc 1
		.amdhsa_float_round_mode_32 0
		.amdhsa_float_round_mode_16_64 0
		.amdhsa_float_denorm_mode_32 3
		.amdhsa_float_denorm_mode_16_64 3
		.amdhsa_dx10_clamp 1
		.amdhsa_ieee_mode 1
		.amdhsa_fp16_overflow 0
		.amdhsa_tg_split 0
		.amdhsa_exception_fp_ieee_invalid_op 0
		.amdhsa_exception_fp_denorm_src 0
		.amdhsa_exception_fp_ieee_div_zero 0
		.amdhsa_exception_fp_ieee_overflow 0
		.amdhsa_exception_fp_ieee_underflow 0
		.amdhsa_exception_fp_ieee_inexact 0
		.amdhsa_exception_int_div_zero 0
	.end_amdhsa_kernel

amdhsa.kernels:
  - .agpr_count:     0
    .args:
      - .actual_access:  read_only
        .address_space:  global
        .offset:         0
        .size:           8
        .value_kind:     global_buffer
      - .actual_access:  read_only
        .address_space:  global
        .offset:         8
        .size:           8
        .value_kind:     global_buffer
      - .actual_access:  read_only
        .address_space:  global
        .offset:         16
        .size:           8
        .value_kind:     global_buffer
      - .actual_access:  read_only
        .address_space:  global
        .offset:         24
        .size:           8
        .value_kind:     global_buffer
      - .actual_access:  write_only
        .address_space:  global
        .offset:         32
        .size:           8
        .value_kind:     global_buffer
      - .actual_access:  write_only
        .address_space:  global
        .offset:         40
        .size:           8
        .value_kind:     global_buffer
      - .actual_access:  write_only
        .address_space:  global
        .offset:         48
        .size:           8
        .value_kind:     global_buffer
      - .actual_access:  write_only
        .address_space:  global
        .offset:         56
        .size:           8
        .value_kind:     global_buffer
      - .actual_access:  write_only
        .address_space:  global
        .offset:         64
        .size:           8
        .value_kind:     global_buffer
      - .actual_access:  write_only
        .address_space:  global
        .offset:         72
        .size:           8
        .value_kind:     global_buffer
      - .actual_access:  write_only
        .address_space:  global
        .offset:         80
        .size:           8
        .value_kind:     global_buffer
      - .actual_access:  write_only
        .address_space:  global
        .offset:         88
        .size:           8
        .value_kind:     global_buffer
      - .actual_access:  write_only
        .address_space:  global
        .offset:         96
        .size:           8
        .value_kind:     global_buffer
      - .actual_access:  write_only
        .address_space:  global
        .offset:         104
        .size:           8
        .value_kind:     global_buffer
      - .actual_access:  write_only
        .address_space:  global
        .offset:         112
        .size:           8
        .value_kind:     global_buffer
    .group_segment_fixed_size: 67584
    .kernarg_segment_align: 8
    .kernarg_segment_size: 120
    .language:       OpenCL C
    .language_version:
      - 2
      - 0
    .max_flat_workgroup_size: 1024
    .name:           _Z6k_sortPKfS0_PKiS2_PiP15HIP_vector_typeIfLj4EEPfS7_S3_S7_S7_S3_S3_S6_S6_
    .private_segment_fixed_size: 0
    .sgpr_count:     35
    .sgpr_spill_count: 0
    .symbol:         _Z6k_sortPKfS0_PKiS2_PiP15HIP_vector_typeIfLj4EEPfS7_S3_S7_S7_S3_S3_S6_S6_.kd
    .uniform_work_group_size: 1
    .uses_dynamic_stack: false
    .vgpr_count:     40
    .vgpr_spill_count: 0
    .wavefront_size: 64
  - .agpr_count:     0
    .args:
      - .actual_access:  read_only
        .address_space:  global
        .offset:         0
        .size:           8
        .value_kind:     global_buffer
      - .actual_access:  read_only
        .address_space:  global
        .offset:         8
        .size:           8
        .value_kind:     global_buffer
      - .actual_access:  read_only
        .address_space:  global
        .offset:         16
        .size:           8
        .value_kind:     global_buffer
      - .actual_access:  read_only
        .address_space:  global
        .offset:         24
        .size:           8
        .value_kind:     global_buffer
      - .actual_access:  read_only
        .address_space:  global
        .offset:         32
        .size:           8
        .value_kind:     global_buffer
      - .actual_access:  read_only
        .address_space:  global
        .offset:         40
        .size:           8
        .value_kind:     global_buffer
      - .actual_access:  read_only
        .address_space:  global
        .offset:         48
        .size:           8
        .value_kind:     global_buffer
      - .actual_access:  write_only
        .address_space:  global
        .offset:         56
        .size:           8
        .value_kind:     global_buffer
    .group_segment_fixed_size: 145952
    .kernarg_segment_align: 8
    .kernarg_segment_size: 64
    .language:       OpenCL C
    .language_version:
      - 2
      - 0
    .max_flat_workgroup_size: 512
    .name:           _Z7k_finalPK15HIP_vector_typeIfLj4EES2_PKiS4_PKfS6_PKDF16_Pf
    .private_segment_fixed_size: 0
    .sgpr_count:     34
    .sgpr_spill_count: 0
    .symbol:         _Z7k_finalPK15HIP_vector_typeIfLj4EES2_PKiS4_PKfS6_PKDF16_Pf.kd
    .uniform_work_group_size: 1
    .uses_dynamic_stack: false
    .vgpr_count:     177
    .vgpr_spill_count: 0
    .wavefront_size: 64
  - .agpr_count:     0
    .args:
      - .actual_access:  read_only
        .address_space:  global
        .offset:         0
        .size:           8
        .value_kind:     global_buffer
      - .actual_access:  read_only
        .address_space:  global
        .offset:         8
        .size:           8
        .value_kind:     global_buffer
      - .actual_access:  read_only
        .address_space:  global
        .offset:         16
        .size:           8
        .value_kind:     global_buffer
      - .actual_access:  read_only
        .address_space:  global
        .offset:         24
        .size:           8
        .value_kind:     global_buffer
      - .actual_access:  read_only
        .address_space:  global
        .offset:         32
        .size:           8
        .value_kind:     global_buffer
      - .actual_access:  read_only
        .address_space:  global
        .offset:         40
        .size:           8
        .value_kind:     global_buffer
      - .actual_access:  read_only
        .address_space:  global
        .offset:         48
        .size:           8
        .value_kind:     global_buffer
      - .actual_access:  read_only
        .address_space:  global
        .offset:         56
        .size:           8
        .value_kind:     global_buffer
      - .actual_access:  read_only
        .address_space:  global
        .offset:         64
        .size:           8
        .value_kind:     global_buffer
      - .address_space:  global
        .offset:         72
        .size:           8
        .value_kind:     global_buffer
      - .actual_access:  read_only
        .address_space:  global
        .offset:         80
        .size:           8
        .value_kind:     global_buffer
      - .actual_access:  read_only
        .address_space:  global
        .offset:         88
        .size:           8
        .value_kind:     global_buffer
      - .actual_access:  read_only
        .address_space:  global
        .offset:         96
        .size:           8
        .value_kind:     global_buffer
      - .actual_access:  write_only
        .address_space:  global
        .offset:         104
        .size:           8
        .value_kind:     global_buffer
      - .address_space:  global
        .offset:         112
        .size:           8
        .value_kind:     global_buffer
      - .actual_access:  write_only
        .address_space:  global
        .offset:         120
        .size:           8
        .value_kind:     global_buffer
      - .actual_access:  write_only
        .address_space:  global
        .offset:         128
        .size:           8
        .value_kind:     global_buffer
      - .actual_access:  write_only
        .address_space:  global
        .offset:         136
        .size:           8
        .value_kind:     global_buffer
      - .actual_access:  write_only
        .address_space:  global
        .offset:         144
        .size:           8
        .value_kind:     global_buffer
    .group_segment_fixed_size: 30384
    .kernarg_segment_align: 8
    .kernarg_segment_size: 152
    .language:       OpenCL C
    .language_version:
      - 2
      - 0
    .max_flat_workgroup_size: 512
    .name:           _Z6k_iterILb1ELb0EEvPKfS1_PKiPK15HIP_vector_typeIfLj4EES7_S1_S1_S3_S1_PfS8_S1_S3_PDF16_PS5_SA_PiSA_SB_
    .private_segment_fixed_size: 0
    .sgpr_count:     102
    .sgpr_spill_count: 0
    .symbol:         _Z6k_iterILb1ELb0EEvPKfS1_PKiPK15HIP_vector_typeIfLj4EES7_S1_S1_S3_S1_PfS8_S1_S3_PDF16_PS5_SA_PiSA_SB_.kd
    .uniform_work_group_size: 1
    .uses_dynamic_stack: false
    .vgpr_count:     216
    .vgpr_spill_count: 0
    .wavefront_size: 64
  - .agpr_count:     0
    .args:
      - .actual_access:  read_only
        .address_space:  global
        .offset:         0
        .size:           8
        .value_kind:     global_buffer
      - .actual_access:  read_only
        .address_space:  global
        .offset:         8
        .size:           8
        .value_kind:     global_buffer
      - .actual_access:  read_only
        .address_space:  global
        .offset:         16
        .size:           8
        .value_kind:     global_buffer
      - .actual_access:  read_only
        .address_space:  global
        .offset:         24
        .size:           8
        .value_kind:     global_buffer
      - .actual_access:  read_only
        .address_space:  global
        .offset:         32
        .size:           8
        .value_kind:     global_buffer
      - .actual_access:  read_only
        .address_space:  global
        .offset:         40
        .size:           8
        .value_kind:     global_buffer
      - .actual_access:  read_only
        .address_space:  global
        .offset:         48
        .size:           8
        .value_kind:     global_buffer
      - .actual_access:  read_only
        .address_space:  global
        .offset:         56
        .size:           8
        .value_kind:     global_buffer
      - .actual_access:  read_only
        .address_space:  global
        .offset:         64
        .size:           8
        .value_kind:     global_buffer
      - .address_space:  global
        .offset:         72
        .size:           8
        .value_kind:     global_buffer
      - .actual_access:  read_only
        .address_space:  global
        .offset:         80
        .size:           8
        .value_kind:     global_buffer
      - .actual_access:  read_only
        .address_space:  global
        .offset:         88
        .size:           8
        .value_kind:     global_buffer
      - .actual_access:  read_only
        .address_space:  global
        .offset:         96
        .size:           8
        .value_kind:     global_buffer
      - .actual_access:  read_only
        .address_space:  global
        .offset:         104
        .size:           8
        .value_kind:     global_buffer
      - .actual_access:  read_only
        .address_space:  global
        .offset:         112
        .size:           8
        .value_kind:     global_buffer
      - .actual_access:  read_only
        .address_space:  global
        .offset:         120
        .size:           8
        .value_kind:     global_buffer
      - .actual_access:  read_only
        .address_space:  global
        .offset:         128
        .size:           8
        .value_kind:     global_buffer
      - .actual_access:  read_only
        .address_space:  global
        .offset:         136
        .size:           8
        .value_kind:     global_buffer
      - .actual_access:  read_only
        .address_space:  global
        .offset:         144
        .size:           8
        .value_kind:     global_buffer
    .group_segment_fixed_size: 5808
    .kernarg_segment_align: 8
    .kernarg_segment_size: 152
    .language:       OpenCL C
    .language_version:
      - 2
      - 0
    .max_flat_workgroup_size: 512
    .name:           _Z6k_iterILb0ELb0EEvPKfS1_PKiPK15HIP_vector_typeIfLj4EES7_S1_S1_S3_S1_PfS8_S1_S3_PDF16_PS5_SA_PiSA_SB_
    .private_segment_fixed_size: 0
    .sgpr_count:     42
    .sgpr_spill_count: 0
    .symbol:         _Z6k_iterILb0ELb0EEvPKfS1_PKiPK15HIP_vector_typeIfLj4EES7_S1_S1_S3_S1_PfS8_S1_S3_PDF16_PS5_SA_PiSA_SB_.kd
    .uniform_work_group_size: 1
    .uses_dynamic_stack: false
    .vgpr_count:     184
    .vgpr_spill_count: 0
    .wavefront_size: 64
  - .agpr_count:     0
    .args:
      - .actual_access:  read_only
        .address_space:  global
        .offset:         0
        .size:           8
        .value_kind:     global_buffer
      - .actual_access:  read_only
        .address_space:  global
        .offset:         8
        .size:           8
        .value_kind:     global_buffer
      - .actual_access:  read_only
        .address_space:  global
        .offset:         16
        .size:           8
        .value_kind:     global_buffer
      - .actual_access:  read_only
        .address_space:  global
        .offset:         24
        .size:           8
        .value_kind:     global_buffer
      - .actual_access:  read_only
        .address_space:  global
        .offset:         32
        .size:           8
        .value_kind:     global_buffer
      - .actual_access:  read_only
        .address_space:  global
        .offset:         40
        .size:           8
        .value_kind:     global_buffer
      - .actual_access:  read_only
        .address_space:  global
        .offset:         48
        .size:           8
        .value_kind:     global_buffer
      - .actual_access:  read_only
        .address_space:  global
        .offset:         56
        .size:           8
        .value_kind:     global_buffer
      - .actual_access:  read_only
        .address_space:  global
        .offset:         64
        .size:           8
        .value_kind:     global_buffer
      - .address_space:  global
        .offset:         72
        .size:           8
        .value_kind:     global_buffer
      - .actual_access:  write_only
        .address_space:  global
        .offset:         80
        .size:           8
        .value_kind:     global_buffer
      - .actual_access:  read_only
        .address_space:  global
        .offset:         88
        .size:           8
        .value_kind:     global_buffer
      - .actual_access:  read_only
        .address_space:  global
        .offset:         96
        .size:           8
        .value_kind:     global_buffer
      - .actual_access:  read_only
        .address_space:  global
        .offset:         104
        .size:           8
        .value_kind:     global_buffer
      - .actual_access:  read_only
        .address_space:  global
        .offset:         112
        .size:           8
        .value_kind:     global_buffer
      - .actual_access:  read_only
        .address_space:  global
        .offset:         120
        .size:           8
        .value_kind:     global_buffer
      - .actual_access:  read_only
        .address_space:  global
        .offset:         128
        .size:           8
        .value_kind:     global_buffer
      - .actual_access:  read_only
        .address_space:  global
        .offset:         136
        .size:           8
        .value_kind:     global_buffer
      - .actual_access:  read_only
        .address_space:  global
        .offset:         144
        .size:           8
        .value_kind:     global_buffer
    .group_segment_fixed_size: 5808
    .kernarg_segment_align: 8
    .kernarg_segment_size: 152
    .language:       OpenCL C
    .language_version:
      - 2
      - 0
    .max_flat_workgroup_size: 512
    .name:           _Z6k_iterILb0ELb1EEvPKfS1_PKiPK15HIP_vector_typeIfLj4EES7_S1_S1_S3_S1_PfS8_S1_S3_PDF16_PS5_SA_PiSA_SB_
    .private_segment_fixed_size: 0
    .sgpr_count:     42
    .sgpr_spill_count: 0
    .symbol:         _Z6k_iterILb0ELb1EEvPKfS1_PKiPK15HIP_vector_typeIfLj4EES7_S1_S1_S3_S1_PfS8_S1_S3_PDF16_PS5_SA_PiSA_SB_.kd
    .uniform_work_group_size: 1
    .uses_dynamic_stack: false
    .vgpr_count:     184
    .vgpr_spill_count: 0
    .wavefront_size: 64
